# speedup vs baseline: 1.0165x; 1.0165x over previous
_Z8k2_fusedPKDF16_PKDv8_DF16_PKfS5_S5_PfPiS6_:
	s_lshl_b32 s3, s2, 2
	s_ashr_i32 s16, s2, 4
	s_and_b32 s12, s3, 48
	s_lshl_b32 s2, s2, 4
	s_and_b32 s13, s2, 48
	s_add_i32 s2, s12, -2
	v_mul_u32_u24_e32 v1, 0x334, v0
	s_movk_i32 s15, 0xffec
	s_add_i32 s3, s13, -2
	v_lshrrev_b32_e32 v84, 2, v0
	v_mul_i32_i24_sdwa v2, v1, s15 dst_sel:DWORD dst_unused:UNUSED_PAD src0_sel:WORD_1 src1_sel:DWORD
	v_add_u32_sdwa v48, s2, v1 dst_sel:DWORD dst_unused:UNUSED_PAD src0_sel:DWORD src1_sel:WORD_1
	s_load_dwordx8 s[4:11], s[0:1], 0x0
	s_load_dwordx4 s[32:35], s[0:1], 0x20
	s_load_dwordx2 s[36:37], s[0:1], 0x38
	v_add3_u32 v49, s3, v84, v2
	v_max_i32_e32 v1, 0, v48
	s_lshl_b32 s14, s16, 12
	v_med3_i32 v2, v49, 0, 63
	v_lshlrev_b32_e32 v1, 6, v1
	v_or3_b32 v1, v1, v2, s14
	v_lshlrev_b32_e32 v2, 5, v1
	v_ashrrev_i32_e32 v3, 31, v2
	v_lshlrev_b32_e32 v85, 4, v0
	s_waitcnt lgkmcnt(0)
	v_lshl_add_u64 v[2:3], v[2:3], 1, s[4:5]
	v_and_b32_e32 v46, 48, v85
	v_mov_b32_e32 v47, 0
	v_or_b32_e32 v54, 0x200, v0
	v_lshl_add_u64 v[2:3], v[2:3], 0, v[46:47]
	v_mul_u32_u24_e32 v1, 0x334, v54
	global_load_dwordx4 v[18:21], v[2:3], off
	v_lshrrev_b32_e32 v86, 2, v54
	v_mul_i32_i24_sdwa v2, v1, s15 dst_sel:DWORD dst_unused:UNUSED_PAD src0_sel:WORD_1 src1_sel:DWORD
	v_add_u32_sdwa v50, s2, v1 dst_sel:DWORD dst_unused:UNUSED_PAD src0_sel:DWORD src1_sel:WORD_1
	v_add3_u32 v51, s3, v86, v2
	v_min_u32_e32 v1, 63, v50
	v_med3_i32 v2, v51, 0, 63
	v_lshlrev_b32_e32 v1, 6, v1
	v_or3_b32 v1, v1, v2, s14
	v_lshlrev_b32_e32 v2, 5, v1
	v_or_b32_e32 v58, 0x400, v0
	v_ashrrev_i32_e32 v3, 31, v2
	v_lshlrev_b32_e32 v87, 4, v54
	v_mul_u32_u24_e32 v1, 0x667, v58
	v_lshl_add_u64 v[2:3], v[2:3], 1, s[4:5]
	v_and_b32_e32 v4, 48, v87
	v_mov_b32_e32 v5, v47
	v_lshrrev_b32_e32 v1, 17, v1
	v_lshl_add_u64 v[2:3], v[2:3], 0, v[4:5]
	v_mul_i32_i24_e32 v4, 0xffffffec, v1
	v_add_u32_e32 v52, s2, v1
	v_lshrrev_b32_e32 v88, 2, v58
	v_add3_u32 v53, s3, v88, v4
	v_min_u32_e32 v1, 63, v52
	v_med3_i32 v4, v53, 0, 63
	v_lshlrev_b32_e32 v1, 6, v1
	v_or3_b32 v1, v1, v4, s14
	v_lshlrev_b32_e32 v4, 5, v1
	v_ashrrev_i32_e32 v5, 31, v4
	v_or_b32_e32 v89, 0x600, v0
	v_lshl_add_u64 v[4:5], v[4:5], 1, s[4:5]
	v_min_u32_e32 v1, 0x63f, v89
	v_lshl_add_u64 v[4:5], v[4:5], 0, v[46:47]
	global_load_dwordx4 v[22:25], v[2:3], off
	global_load_dwordx4 v[26:29], v[4:5], off
	v_lshrrev_b32_e32 v2, 2, v1
	v_add_u32_e32 v2, s3, v2
	s_add_i32 s15, s12, 17
	v_add_u32_e32 v55, 0xfffffe84, v2
	s_min_u32 s2, s15, 63
	v_min_u32_e32 v2, 63, v55
	v_lshl_or_b32 v2, s2, 6, v2
	v_or_b32_e32 v2, s14, v2
	v_lshlrev_b32_e32 v2, 5, v2
	v_ashrrev_i32_e32 v3, 31, v2
	v_lshlrev_b32_e32 v1, 4, v1
	v_lshl_add_u64 v[2:3], v[2:3], 1, s[4:5]
	v_and_b32_e32 v4, 48, v1
	v_mov_b32_e32 v5, v47
	v_min_u32_e32 v1, 0x47f, v58
	v_lshrrev_b32_e32 v164, 1, v0
	v_lshl_add_u64 v[2:3], v[2:3], 0, v[4:5]
	v_lshlrev_b32_e32 v90, 4, v1
	v_and_b32_e32 v162, 16, v164
	global_load_dwordx4 v[30:33], v[2:3], off
	global_load_dwordx4 v[34:37], v85, s[6:7]
	global_load_dwordx4 v[38:41], v87, s[6:7]
	global_load_dwordx4 v[42:45], v90, s[6:7]
	s_nop 0
	global_load_dwordx4 v[2:5], v162, s[8:9]
	global_load_dwordx4 v[6:9], v162, s[8:9] offset:32
	global_load_dwordx4 v[10:13], v162, s[8:9] offset:64
	global_load_dwordx4 v[14:17], v162, s[8:9] offset:96
	v_or_b32_e32 v48, v48, v49
	v_cmp_gt_u32_e32 vcc, 64, v48
	v_or_b32_e32 v48, v50, v51
	v_cmp_gt_u32_e64 s[2:3], 64, v48
	v_or_b32_e32 v48, v52, v53
	v_and_b32_e32 v1, 63, v0
	v_and_b32_e32 v165, 31, v0
	v_cmp_gt_u32_e64 s[4:5], 64, v48
	v_or_b32_e32 v48, s15, v55
	v_lshrrev_b32_e32 v163, 6, v0
	v_cmp_gt_u32_e64 s[6:7], 64, v48
	v_and_b32_e32 v48, 0xe0, v0
	s_lshr_b32 s8, s12, 1
	v_lshl_or_b32 v62, s13, 4, v48
	v_lshrrev_b32_e32 v48, 8, v0
	v_or_b32_e32 v48, s8, v48
	v_lshlrev_b32_e32 v48, 10, v48
	v_or3_b32 v48, v62, v48, v165
	v_mul_u32_u24_e32 v48, 10, v48
	v_lshlrev_b32_e32 v59, 2, v48
	v_lshrrev_b32_e32 v48, 8, v54
	v_or_b32_e32 v48, s8, v48
	v_lshlrev_b32_e32 v48, 10, v48
	v_or3_b32 v48, v62, v48, v165
	v_mul_lo_u32 v48, v48, 10
	v_mov_b32_e32 v49, v47
	v_lshl_add_u64 v[48:49], v[48:49], 2, s[10:11]
	global_load_dwordx4 v[50:53], v59, s[10:11] offset:16
	global_load_dwordx4 v[66:69], v59, s[10:11]
	global_load_dwordx2 v[154:155], v[48:49], off offset:32
	global_load_dwordx4 v[54:57], v[48:49], off offset:16
	global_load_dwordx2 v[156:157], v59, s[10:11] offset:32
	global_load_dwordx4 v[70:73], v[48:49], off
	v_lshrrev_b32_e32 v48, 8, v58
	v_lshrrev_b32_e32 v63, 8, v89
	v_or_b32_e32 v48, s8, v48
	v_or_b32_e32 v63, s8, v63
	v_lshlrev_b32_e32 v48, 10, v48
	v_lshlrev_b32_e32 v63, 10, v63
	v_or3_b32 v48, v62, v48, v165
	v_or3_b32 v62, v62, v63, v165
	v_mul_lo_u32 v48, v48, 10
	v_mov_b32_e32 v49, v47
	v_mul_lo_u32 v62, v62, 10
	v_mov_b32_e32 v63, v47
	v_lshl_add_u64 v[48:49], v[48:49], 2, s[10:11]
	v_lshl_add_u64 v[82:83], v[62:63], 2, s[10:11]
	global_load_dwordx4 v[58:61], v[48:49], off offset:16
	global_load_dwordx4 v[74:77], v[48:49], off
	global_load_dwordx2 v[158:159], v[82:83], off offset:32
	global_load_dwordx4 v[62:65], v[82:83], off offset:16
	global_load_dwordx2 v[160:161], v[48:49], off offset:32
	global_load_dwordx4 v[78:81], v[82:83], off
	s_movk_i32 s8, 0x50
	s_waitcnt vmcnt(22)
	v_cndmask_b32_e32 v19, 0, v19, vcc
	v_cndmask_b32_e32 v18, 0, v18, vcc
	v_cndmask_b32_e32 v21, 0, v21, vcc
	v_cndmask_b32_e32 v20, 0, v20, vcc
	v_mad_u32_u24 v47, v84, s8, v46
	ds_write_b128 v47, v[18:21]
	s_waitcnt vmcnt(21)
	v_cndmask_b32_e64 v19, 0, v23, s[2:3]
	v_cndmask_b32_e64 v18, 0, v22, s[2:3]
	v_cndmask_b32_e64 v21, 0, v25, s[2:3]
	v_cndmask_b32_e64 v20, 0, v24, s[2:3]
	v_mad_u32_u24 v22, v86, s8, v46
	ds_write_b128 v22, v[18:21]
	s_waitcnt vmcnt(20)
	v_cndmask_b32_e64 v19, 0, v27, s[4:5]
	v_cndmask_b32_e64 v18, 0, v26, s[4:5]
	v_cndmask_b32_e64 v21, 0, v29, s[4:5]
	v_cndmask_b32_e64 v20, 0, v28, s[4:5]
	v_mad_u32_u24 v22, v88, s8, v46
	ds_write_b128 v22, v[18:21]
	v_lshrrev_b32_e32 v22, 2, v89
	s_waitcnt vmcnt(19)
	v_cndmask_b32_e64 v19, 0, v31, s[6:7]
	v_cndmask_b32_e64 v18, 0, v30, s[6:7]
	v_cndmask_b32_e64 v21, 0, v33, s[6:7]
	v_cndmask_b32_e64 v20, 0, v32, s[6:7]
	v_mad_u32_u24 v22, v22, s8, v46
	ds_write_b128 v22, v[18:21]
	s_waitcnt vmcnt(18)
	ds_write_b128 v85, v[34:37] offset:57920
	s_waitcnt vmcnt(17)
	ds_write_b128 v87, v[38:41] offset:57920
	s_waitcnt vmcnt(16)
	ds_write_b128 v90, v[42:45] offset:57920
	v_lshlrev_b32_e32 v18, 4, v1
	s_waitcnt lgkmcnt(0)
	s_barrier
	v_add_u32_e32 v19, 0xe240, v18
	ds_read_b128 v[150:153], v18 offset:57920
	ds_read_b128 v[146:149], v18 offset:58944
	ds_read_b128 v[142:145], v18 offset:59968
	ds_read_b128 v[138:141], v18 offset:60992
	ds_read_b128 v[134:137], v18 offset:62016
	ds_read_b128 v[130:133], v18 offset:63040
	ds_read_b128 v[126:129], v18 offset:64064
	ds_read_b128 v[122:125], v18 offset:65088
	ds_read_b128 v[118:121], v19 offset:8192
	ds_read_b128 v[114:117], v19 offset:9216
	ds_read_b128 v[110:113], v19 offset:10240
	ds_read_b128 v[106:109], v19 offset:11264
	ds_read_b128 v[102:105], v19 offset:12288
	ds_read_b128 v[98:101], v19 offset:13312
	ds_read_b128 v[94:97], v19 offset:14336
	ds_read_b128 v[90:93], v19 offset:15360
	ds_read_b128 v[86:89], v19 offset:16384
	ds_read_b128 v[82:85], v19 offset:17408
	v_lshl_or_b32 v166, v163, 5, v165
	v_mul_u32_u24_e32 v18, 0xe39, v166
	v_lshrrev_b32_e32 v168, 16, v18
	s_movk_i32 s4, 0xffee
	v_mad_i32_i24 v169, v168, s4, v166
	v_min_u32_e32 v19, 0x43, v166
	v_mad_u32_u24 v18, v168, 20, v169
	v_or_b32_e32 v165, 0x100, v19
	s_movk_i32 s2, 0xc0
	v_mul_lo_u32 v18, v18, s8
	v_mul_u32_u24_e32 v19, 0xe39, v165
	v_cmp_gt_u32_e32 vcc, s2, v0
	s_movk_i32 s2, 0xbf
	v_lshrrev_b32_e32 v167, 16, v19
	v_cmp_lt_u32_e64 s[2:3], s2, v0
	v_add_u32_e32 v171, v18, v162
	s_and_saveexec_b64 s[6:7], s[2:3]
	s_xor_b64 s[2:3], exec, s[6:7]
	s_cbranch_execz .LBB1_2
	ds_read_b128 v[34:37], v171
	ds_read_b128 v[38:41], v171 offset:32
	ds_read_b128 v[42:45], v171 offset:80
	ds_read_b128 v[46:49], v171 offset:112
	ds_read_b128 v[172:175], v171 offset:160
	ds_read_b128 v[176:179], v171 offset:192
	ds_read_b128 v[180:183], v171 offset:1600
	ds_read_b128 v[184:187], v171 offset:1632
	ds_read_b128 v[188:191], v171 offset:1680
	s_waitcnt vmcnt(12) lgkmcnt(8)
	v_mfma_f32_32x32x16_f16 v[18:33], v[150:153], v[34:37], v[2:17]
	s_waitcnt lgkmcnt(7)
	v_mfma_f32_32x32x16_f16 v[18:33], v[146:149], v[38:41], v[18:33]
	ds_read_b128 v[34:37], v171 offset:1712
	s_waitcnt lgkmcnt(7)
	v_mfma_f32_32x32x16_f16 v[18:33], v[142:145], v[42:45], v[18:33]
	ds_read_b128 v[38:41], v171 offset:1760
	s_waitcnt lgkmcnt(7)
	v_mfma_f32_32x32x16_f16 v[18:33], v[138:141], v[46:49], v[18:33]
	ds_read_b128 v[42:45], v171 offset:1792
	s_waitcnt lgkmcnt(7)
	v_mfma_f32_32x32x16_f16 v[18:33], v[134:137], v[172:175], v[18:33]
	ds_read_b128 v[46:49], v171 offset:3200
	s_waitcnt lgkmcnt(7)
	v_mfma_f32_32x32x16_f16 v[18:33], v[130:133], v[176:179], v[18:33]
	ds_read_b128 v[172:175], v171 offset:3232
	s_waitcnt lgkmcnt(7)
	v_mfma_f32_32x32x16_f16 v[18:33], v[126:129], v[180:183], v[18:33]
	ds_read_b128 v[176:179], v171 offset:3280
	s_waitcnt lgkmcnt(7)
	v_mfma_f32_32x32x16_f16 v[18:33], v[122:125], v[184:187], v[18:33]
	ds_read_b128 v[180:183], v171 offset:3312
	s_waitcnt lgkmcnt(7)
	v_mfma_f32_32x32x16_f16 v[18:33], v[118:121], v[188:191], v[18:33]
	ds_read_b128 v[184:187], v171 offset:3360
	s_waitcnt lgkmcnt(7)
	v_mfma_f32_32x32x16_f16 v[18:33], v[114:117], v[34:37], v[18:33]
	ds_read_b128 v[188:191], v171 offset:3392
	s_waitcnt lgkmcnt(7)
	v_mfma_f32_32x32x16_f16 v[18:33], v[110:113], v[38:41], v[18:33]
	s_waitcnt lgkmcnt(6)
	v_mfma_f32_32x32x16_f16 v[18:33], v[106:109], v[42:45], v[18:33]
	s_waitcnt lgkmcnt(5)
	v_mfma_f32_32x32x16_f16 v[18:33], v[102:105], v[46:49], v[18:33]
	s_waitcnt lgkmcnt(4)
	v_mfma_f32_32x32x16_f16 v[18:33], v[98:101], v[172:175], v[18:33]
	s_waitcnt lgkmcnt(3)
	v_mfma_f32_32x32x16_f16 v[18:33], v[94:97], v[176:179], v[18:33]
	s_waitcnt lgkmcnt(2)
	v_mfma_f32_32x32x16_f16 v[18:33], v[90:93], v[180:183], v[18:33]
	s_waitcnt lgkmcnt(1)
	v_mfma_f32_32x32x16_f16 v[18:33], v[86:89], v[184:187], v[18:33]
	s_waitcnt lgkmcnt(0)
	v_mfma_f32_32x32x16_f16 v[18:33], v[82:85], v[188:191], v[18:33]
	v_mov_b32_e32 v49, v17
	v_mov_b32_e32 v48, v16
	v_mov_b32_e32 v47, v15
	v_mov_b32_e32 v46, v14
	v_mov_b32_e32 v45, v13
	v_mov_b32_e32 v44, v12
	v_mov_b32_e32 v43, v11
	v_mov_b32_e32 v42, v10
	v_mov_b32_e32 v41, v9
	v_mov_b32_e32 v40, v8
	v_mov_b32_e32 v39, v7
	v_mov_b32_e32 v38, v6
	v_mov_b32_e32 v37, v5
	v_mov_b32_e32 v36, v4
	v_mov_b32_e32 v35, v3
	v_mov_b32_e32 v34, v2

.LBB1_12:
	s_or_b64 exec, exec, s[2:3]
	v_cmp_gt_u32_e32 vcc, 64, v0
	s_waitcnt lgkmcnt(0)
	s_barrier
	s_and_saveexec_b64 s[2:3], vcc
	s_cbranch_execz .LBB1_25
	s_mov_b64 s[12:13], s[32:33]
	s_mov_b64 s[14:15], s[34:35]
	s_mov_b64 s[18:19], s[36:37]
	v_cmp_gt_u32_e64 s[2:3], 10, v0
	s_movk_i32 s4, 0xffe0
	s_nop 0
	v_cndmask_b32_e64 v1, 9, v0, s[2:3]
	v_lshlrev_b32_e32 v2, 2, v1
	s_waitcnt lgkmcnt(0)
	global_load_dword v1, v2, s[12:13]
	v_add_u32_e32 v8, 0x14a40, v2
	v_add_u32_e32 v9, 0x400, v8
	ds_read2_b32 v[2:3], v8 offset1:10
	ds_read2_b32 v[4:5], v8 offset0:20 offset1:30
	ds_read2_b32 v[6:7], v8 offset0:40 offset1:50
	ds_read2_b32 v[10:11], v8 offset0:60 offset1:70
	ds_read2_b32 v[12:13], v8 offset0:80 offset1:90
	ds_read2_b32 v[14:15], v8 offset0:100 offset1:110
	ds_read2_b32 v[16:17], v8 offset0:120 offset1:130
	ds_read2_b32 v[18:19], v8 offset0:140 offset1:150
	ds_read2_b32 v[20:21], v8 offset0:160 offset1:170
	ds_read2_b32 v[22:23], v8 offset0:180 offset1:190
	ds_read2_b32 v[24:25], v8 offset0:200 offset1:210
	ds_read2_b32 v[26:27], v8 offset0:220 offset1:230
	ds_read2_b32 v[28:29], v8 offset0:240 offset1:250
	s_waitcnt lgkmcnt(9)
	v_add_f32_e32 v2, 0, v2
	v_add_f32_e32 v2, v2, v3
	v_add_f32_e32 v2, v2, v4
	v_add_f32_e32 v2, v2, v5
	v_add_f32_e32 v2, v2, v6
	v_add_f32_e32 v2, v2, v7
	v_add_f32_e32 v2, v2, v10
	v_add_f32_e32 v2, v2, v11
	ds_read2_b32 v[30:31], v9 offset0:4 offset1:14
	ds_read2_b32 v[32:33], v9 offset0:24 offset1:34
	ds_read2_b32 v[34:35], v9 offset0:44 offset1:54
	s_waitcnt lgkmcnt(8)
	v_add_f32_e32 v2, v2, v12
	v_add_f32_e32 v2, v2, v13
	v_add_f32_e32 v2, v2, v14
	v_add_f32_e32 v2, v2, v15
	v_add_f32_e32 v2, v2, v16
	v_add_f32_e32 v2, v2, v17
	v_add_f32_e32 v2, v2, v18
	v_add_f32_e32 v2, v2, v19
	s_waitcnt lgkmcnt(4)
	v_add_f32_e32 v2, v2, v20
	v_add_f32_e32 v2, v2, v21
	v_add_f32_e32 v2, v2, v22
	v_add_f32_e32 v2, v2, v23
	v_add_f32_e32 v2, v2, v24
	v_add_f32_e32 v2, v2, v25
	v_add_f32_e32 v2, v2, v26
	v_add_f32_e32 v2, v2, v27
	s_waitcnt lgkmcnt(0)
	v_add_f32_e32 v2, v2, v28
	v_add_f32_e32 v2, v2, v29
	v_add_f32_e32 v2, v2, v30
	v_add_f32_e32 v2, v2, v31
	v_add_f32_e32 v2, v2, v32
	v_add_f32_e32 v2, v2, v33
	v_add_f32_e32 v2, v2, v34
	v_add_f32_e32 v2, v2, v35
	v_cvt_f64_f32_e32 v[2:3], v2
	v_ldexp_f64 v[2:3], v[2:3], 36
	v_rndne_f64_e32 v[2:3], v[2:3]
	v_ldexp_f64 v[4:5], v[2:3], s4
	v_floor_f64_e32 v[4:5], v[4:5]
	v_fmac_f64_e32 v[2:3], 0xc1f00000, v[4:5]
	v_cvt_u32_f64_e32 v2, v[2:3]
	v_cvt_i32_f64_e32 v3, v[4:5]
	v_lshlrev_b64 v[2:3], 5, v[2:3]
	v_or_b32_e32 v2, 1, v2
	v_mov_b64_e32 v[4:5], 0
	s_and_saveexec_b64 s[4:5], s[2:3]
	s_cbranch_execz .LBB1_15
	s_mul_i32 s6, s16, 10
	s_ashr_i32 s7, s6, 31
	s_lshl_b64 s[6:7], s[6:7], 3
	s_add_u32 s6, s14, s6
	s_addc_u32 s7, s15, s7
	v_lshlrev_b32_e32 v4, 3, v0
	global_atomic_add_x2 v[4:5], v4, v[2:3], s[6:7] sc0

.LBB1_22:
	s_andn2_b64 vcc, exec, s[6:7]
	s_cbranch_vccnz .LBB1_25
	v_add_f32_e32 v1, v1, v2
	v_mov_b32_e32 v2, 0xff61b1e6
	v_cndmask_b32_e64 v1, v2, v1, s[2:3]
	s_mov_b32 s0, 0x3fb8aa3b
	s_nop 0
	v_max_f32_dpp v5, v1, v1 row_ror:8 row_mask:0xf bank_mask:0xf
	s_nop 1
	v_max_f32_dpp v5, v5, v5 row_ror:4 row_mask:0xf bank_mask:0xf
	s_nop 1
	v_max_f32_dpp v5, v5, v5 quad_perm:[2,3,0,1] row_mask:0xf bank_mask:0xf
	s_nop 1
	v_max_f32_dpp v2, v5, v5 quad_perm:[1,0,3,2] row_mask:0xf bank_mask:0xf
	v_sub_f32_e32 v1, v1, v2
	v_mul_f32_e32 v2, 0x3fb8aa3b, v1
	v_fma_f32 v5, v1, s0, -v2
	v_rndne_f32_e32 v8, v2
	v_fmamk_f32 v5, v1, 0x32a5705f, v5
	v_sub_f32_e32 v2, v2, v8
	v_add_f32_e32 v2, v2, v5
	v_exp_f32_e32 v2, v2
	v_cvt_i32_f32_e32 v5, v8
	s_mov_b32 s0, 0xc2ce8ed0
	v_cmp_ngt_f32_e32 vcc, s0, v1
	s_mov_b32 s0, 0x42b17218
	v_ldexp_f32 v2, v2, v5
	v_cndmask_b32_e32 v2, 0, v2, vcc
	v_mov_b32_e32 v5, 0x7f800000
	v_cmp_nlt_f32_e32 vcc, s0, v1
	s_nop 1
	v_cndmask_b32_e32 v1, v5, v2, vcc
	v_cndmask_b32_e64 v2, 0, v1, s[2:3]
	s_nop 1
	v_add_f32_dpp v2, v2, v2 row_ror:8 row_mask:0xf bank_mask:0xf
	s_nop 1
	v_add_f32_dpp v2, v2, v2 row_ror:4 row_mask:0xf bank_mask:0xf
	s_nop 1
	v_add_f32_dpp v2, v2, v2 quad_perm:[2,3,0,1] row_mask:0xf bank_mask:0xf
	s_nop 1
	v_add_f32_dpp v2, v2, v2 quad_perm:[1,0,3,2] row_mask:0xf bank_mask:0xf
	s_and_b64 exec, exec, s[2:3]
	s_cbranch_execz .LBB1_25
	v_div_scale_f32 v3, s[0:1], v2, v2, v1
	v_rcp_f32_e32 v4, v3
	v_div_scale_f32 v5, vcc, v1, v2, v1
	v_fma_f32 v6, -v3, v4, 1.0
	v_fmac_f32_e32 v4, v6, v4
	v_mul_f32_e32 v6, v5, v4
	v_fma_f32 v7, -v3, v6, v5
	v_fmac_f32_e32 v6, v7, v4
	v_fma_f32 v3, -v3, v6, v5
	v_div_fmas_f32 v3, v3, v4, v6
	v_div_fixup_f32 v2, v3, v2, v1
	v_mad_u64_u32 v[0:1], s[0:1], s16, 10, v[0:1]
	v_ashrrev_i32_e32 v1, 31, v0
	v_lshl_add_u64 v[0:1], v[0:1], 2, s[18:19]
	global_store_dword v[0:1], v2, off
